# adds: moe2 YS epilogue stores non-temporal (keeps shared expert weights in L2)
# speedup vs baseline: 1.0301x; 1.0068x over previous
; __device__ __forceinline__ uint4 pack8(const float* v) { uint4 r; r.x = pack2(v[0], v[1]); r.y = pack2(v[2], v[3]); r.z = pack2(v[4], v[5]); r.w = pack2(v[6], v[7]); return r; }
;     template <int BN> __device__ __forceinline__ void rows3(const float* Ct, int cstr, int mi) {
;         for (int id_ = threadIdx.x; id_ < 64 * (BN / 8); id_ += NTHR) {
;             const int lr = id_ / (BN / 8), c = (id_ % (BN / 8)) * 8;
;             const int r = (lr >> 5) * 96 + mi * 32 + (lr & 31);
;             const int pidx = rp[r];
;             if (pidx >= 0) {
;                 const float g = GATE[r];
;                 float v[8]; ld8(Ct + lr * cstr + c, v);
; #pragma unroll
;                 for (int j = 0; j < 8; ++j) v[j] *= g;
;                 *(uint4*)&YS[(size_t)pidx * 1024 + col0 + c] = pack8(v);
;             }
;         }
;     }
.LBB0_1616:
	v_lshrrev_b32_e32 v71, 10, v70
	v_mul_u32_u24_e32 v71, 0x60, v71
	v_and_or_b32 v71, v68, 31, v71
	v_lshl_add_u32 v72, v71, 2, s26
	ds_read_b32 v198, v72
	s_waitcnt lgkmcnt(0)
	v_cmp_lt_i32_e32 vcc, -1, v198
	s_and_saveexec_b64 s[14:15], vcc
	s_cbranch_execz .LBB0_1615
	v_lshl_add_u32 v71, v71, 2, s25
	ds_read_b32 v80, v71
	ds_read_b128 v[72:75], v69
	ds_read_b128 v[76:79], v69 offset:16
	s_waitcnt lgkmcnt(1)
	v_pk_mul_f32 v[72:73], v[80:81], v[72:73] op_sel_hi:[0,1]
	v_pk_mul_f32 v[74:75], v[80:81], v[74:75] op_sel_hi:[0,1]
	s_waitcnt lgkmcnt(0)
	v_pk_mul_f32 v[76:77], v[80:81], v[76:77] op_sel_hi:[0,1]
	v_pk_mul_f32 v[78:79], v[80:81], v[78:79] op_sel_hi:[0,1]
	v_cvt_pk_bf16_f32 v72, v72, v73
	v_cvt_pk_bf16_f32 v73, v74, v75
	v_cvt_pk_bf16_f32 v74, v76, v77
	v_lshlrev_b64 v[76:77], 11, v[198:199]
	v_cvt_pk_bf16_f32 v75, v78, v79
	v_lshl_add_u64 v[76:77], v[66:67], 0, v[76:77]
	global_store_dwordx4 v[76:77], v[72:75], off nt
	s_branch .LBB0_1615

; __device__ __forceinline__ uint4 pack8(const float* v) { uint4 r; r.x = pack2(v[0], v[1]); r.y = pack2(v[2], v[3]); r.z = pack2(v[4], v[5]); r.w = pack2(v[6], v[7]); return r; }
;     template <int BN> __device__ __forceinline__ void rows3(const float* Ct, int cstr, int mi) {
;         for (int id_ = threadIdx.x; id_ < 64 * (BN / 8); id_ += NTHR) {
;             const int lr = id_ / (BN / 8), c = (id_ % (BN / 8)) * 8;
;             const int r = (lr >> 5) * 96 + mi * 32 + (lr & 31);
;             const int pidx = rp[r];
;             if (pidx >= 0) {
;                 const float g = GATE[r];
;                 float v[8]; ld8(Ct + lr * cstr + c, v);
; #pragma unroll
;                 for (int j = 0; j < 8; ++j) v[j] *= g;
;                 *(uint4*)&YS[(size_t)pidx * 1024 + col0 + c] = pack8(v);
;             }
;         }
;     }
.LBB0_1620:
	v_lshrrev_b32_e32 v37, 10, v36
	v_mul_u32_u24_e32 v37, 0x60, v37
	v_and_or_b32 v37, v34, 31, v37
	v_lshl_add_u32 v38, v37, 2, s26
	ds_read_b32 v198, v38 offset:128
	s_waitcnt lgkmcnt(0)
	v_cmp_lt_i32_e32 vcc, -1, v198
	s_and_saveexec_b64 s[14:15], vcc
	s_cbranch_execz .LBB0_1619
	v_lshl_add_u32 v37, v37, 2, s25
	ds_read_b32 v46, v37 offset:128
	ds_read_b128 v[38:41], v35
	ds_read_b128 v[42:45], v35 offset:16
	s_waitcnt lgkmcnt(1)
	v_pk_mul_f32 v[38:39], v[46:47], v[38:39] op_sel_hi:[0,1]
	v_pk_mul_f32 v[40:41], v[46:47], v[40:41] op_sel_hi:[0,1]
	s_waitcnt lgkmcnt(0)
	v_pk_mul_f32 v[42:43], v[46:47], v[42:43] op_sel_hi:[0,1]
	v_pk_mul_f32 v[44:45], v[46:47], v[44:45] op_sel_hi:[0,1]
	v_cvt_pk_bf16_f32 v38, v38, v39
	v_cvt_pk_bf16_f32 v39, v40, v41
	v_cvt_pk_bf16_f32 v40, v42, v43
	v_lshlrev_b64 v[42:43], 11, v[198:199]
	v_cvt_pk_bf16_f32 v41, v44, v45
	v_lshl_add_u64 v[42:43], v[66:67], 0, v[42:43]
	global_store_dwordx4 v[42:43], v[38:41], off nt
	s_branch .LBB0_1619

; __device__ __forceinline__ uint4 pack8(const float* v) { uint4 r; r.x = pack2(v[0], v[1]); r.y = pack2(v[2], v[3]); r.z = pack2(v[4], v[5]); r.w = pack2(v[6], v[7]); return r; }
;     template <int BN> __device__ __forceinline__ void rows3(const float* Ct, int cstr, int mi) {
;         for (int id_ = threadIdx.x; id_ < 64 * (BN / 8); id_ += NTHR) {
;             const int lr = id_ / (BN / 8), c = (id_ % (BN / 8)) * 8;
;             const int r = (lr >> 5) * 96 + mi * 32 + (lr & 31);
;             const int pidx = rp[r];
;             if (pidx >= 0) {
;                 const float g = GATE[r];
;                 float v[8]; ld8(Ct + lr * cstr + c, v);
; #pragma unroll
;                 for (int j = 0; j < 8; ++j) v[j] *= g;
;                 *(uint4*)&YS[(size_t)pidx * 1024 + col0 + c] = pack8(v);
;             }
;         }
;     }
.LBB0_1624:
	v_lshrrev_b32_e32 v5, 10, v4
	v_mul_u32_u24_e32 v5, 0x60, v5
	v_and_or_b32 v5, v2, 31, v5
	v_lshl_add_u32 v6, v5, 2, s26
	ds_read_b32 v198, v6 offset:256
	s_waitcnt lgkmcnt(0)
	v_cmp_lt_i32_e32 vcc, -1, v198
	s_and_saveexec_b64 s[14:15], vcc
	s_cbranch_execz .LBB0_1623
	v_lshl_add_u32 v5, v5, 2, s25
	ds_read_b32 v14, v5 offset:256
	ds_read_b128 v[6:9], v3
	ds_read_b128 v[10:13], v3 offset:16
	s_waitcnt lgkmcnt(1)
	v_pk_mul_f32 v[6:7], v[14:15], v[6:7] op_sel_hi:[0,1]
	v_pk_mul_f32 v[8:9], v[14:15], v[8:9] op_sel_hi:[0,1]
	s_waitcnt lgkmcnt(0)
	v_pk_mul_f32 v[10:11], v[14:15], v[10:11] op_sel_hi:[0,1]
	v_pk_mul_f32 v[12:13], v[14:15], v[12:13] op_sel_hi:[0,1]
	v_cvt_pk_bf16_f32 v6, v6, v7
	v_cvt_pk_bf16_f32 v7, v8, v9
	v_cvt_pk_bf16_f32 v8, v10, v11
	v_lshlrev_b64 v[10:11], 11, v[198:199]
	v_cvt_pk_bf16_f32 v9, v12, v13
	v_lshl_add_u64 v[10:11], v[66:67], 0, v[10:11]
	global_store_dwordx4 v[10:11], v[6:9], off nt
	s_branch .LBB0_1623
